# F: MoE-down tail expert-count loads issued together; I: grid barrier: non-leader workgroups poll the top-level release generation directly instead of the per-XCD relay word
# baseline (speedup 1.0000x reference)
; __device__ __forceinline__ unsigned xb_ld(unsigned* p)              { return __hip_atomic_load(p, __ATOMIC_RELAXED, __HIP_MEMORY_SCOPE_AGENT); }
; __device__ __forceinline__ unsigned xb_add(unsigned* p, unsigned v) { return __hip_atomic_fetch_add(p, v, __ATOMIC_RELAXED, __HIP_MEMORY_SCOPE_AGENT); }
; #define XB_SPIN(cond, bar) do { unsigned _sp = 0; while (cond) { __builtin_amdgcn_s_sleep(1); \
;     if ((++_sp & 255u) == 0u) { if (xb_ld(&(bar)[XB_TMO])) break; if (_sp > XB_SPIN_CAP) { atomicAdd(&(bar)[XB_TMO], 1u); break; } } } } while (0)
; __device__ __forceinline__ void xcd_barrier(const XcdBarrier& b) {
;     ...
;     if (threadIdx.x == 0) {
;         unsigned* bar = b.bar;
;         __builtin_amdgcn_s_waitcnt(0);
;         unsigned nloc = b.st[0], nx = b.st[1];
;         if (nloc == 0u) { xcd_barrier_complete(bar, b.x, nloc, nx); b.st[0] = nloc; b.st[1] = nx; }
;         const unsigned old = xb_add(&bar[XB_XSUB(b.x)], 1u);
;         const unsigned gen = old / nloc;
;         if (old + 1u == (gen + 1u) * nloc) {
;             __builtin_amdgcn_fence(__ATOMIC_RELEASE, "agent");
;             asm volatile("s_waitcnt vmcnt(0)" ::: "memory");
;             const unsigned og = xb_add(&bar[XB_TOP], 1u);
;             const unsigned tg = og / nx;
;             if (og + 1u == (tg + 1u) * nx) xb_add(&bar[XB_TOPGEN], 1u);
;             else XB_SPIN(xb_ld(&bar[XB_TOPGEN]) == tg, bar);
;             __builtin_amdgcn_fence(__ATOMIC_ACQUIRE, "agent");
;             xb_add(&bar[XB_XGEN(b.x)], 1u);
;             asm volatile("s_waitcnt vmcnt(0)" ::: "memory");
;         } else {
;             XB_SPIN(xb_ld(&bar[XB_XGEN(b.x)]) == gen, bar);
;             __builtin_amdgcn_fence(__ATOMIC_ACQUIRE, "agent");
;             asm volatile("s_waitcnt vmcnt(0)" ::: "memory");
;         }
.LBB0_245:
	v_readlane_b32 s4, v252, 23
	v_readlane_b32 s5, v252, 24
	v_cvt_f32_u32_e32 v1, v4
	v_sub_u32_e32 v6, 0, v4
	v_rcp_iflag_f32_e32 v1, v1
	s_nop 1
	global_atomic_add v5, v3, v212, s[4:5] sc0
	v_mul_f32_e32 v1, 0x4f7ffffe, v1
	v_cvt_u32_f32_e32 v1, v1
	v_mul_lo_u32 v6, v6, v1
	v_mul_hi_u32 v6, v1, v6
	v_add_u32_e32 v1, v1, v6
	s_waitcnt vmcnt(0)
	v_mul_hi_u32 v1, v5, v1
	v_mul_lo_u32 v6, v1, v4
	v_sub_u32_e32 v6, v5, v6
	v_add_u32_e32 v7, 1, v1
	v_cmp_ge_u32_e32 vcc, v6, v4
	v_add_u32_e32 v5, 1, v5
	s_nop 0
	v_cndmask_b32_e32 v1, v1, v7, vcc
	v_sub_u32_e32 v7, v6, v4
	v_cndmask_b32_e32 v6, v6, v7, vcc
	v_add_u32_e32 v7, 1, v1
	v_cmp_ge_u32_e32 vcc, v6, v4
	s_nop 1
	v_cndmask_b32_e32 v1, v1, v7, vcc
	v_mul_lo_u32 v6, v4, v1
	v_add_u32_e32 v4, v6, v4
	v_cmp_ne_u32_e32 vcc, v5, v4
	s_and_saveexec_b64 s[4:5], vcc
	s_xor_b64 s[4:5], exec, s[4:5]
	s_cbranch_execz .LBB0_259
	v_readlane_b32 s6, v252, 29
	v_readlane_b32 s7, v252, 30
	s_waitcnt lgkmcnt(0)
	s_nop 3
	global_load_dword v2, v3, s[6:7] sc1
	s_waitcnt vmcnt(0)
	v_cmp_eq_u32_e32 vcc, v2, v1
	s_and_saveexec_b64 s[6:7], vcc
	s_cbranch_execz .LBB0_258
	s_mov_b32 s8, 1
	s_mov_b64 s[14:15], 0
	s_branch .LBB0_249

; __device__ __forceinline__ int otid() { int t = threadIdx.x; asm volatile("" : "+v"(t)); return t; }
; #pragma unroll
;     for (int e = 0; e < 32; ++e) t += (cnt[e] + 255) >> 8;
;     return t; }
; __device__ __forceinline__ void side_range(const Params& p, int layer, int beg, int end, int first, int stride) {
;     const int lane = otid() & 63;
; #pragma unroll 1
;     for (int it0 = beg + first; it0 < end; it0 += 2 * stride) {
;         f32x4 v0[8], v1[8]; const int it1 = it0 + stride; const bool two = it1 < end;
;         moe_item_copy_nt(p, layer, it0, lane, v0, false); if (two) moe_item_copy_nt(p, layer, it1, lane, v1, false);
;         moe_item_copy_nt(p, layer, it0, lane, v0, true); if (two) moe_item_copy_nt(p, layer, it1, lane, v1, true);
;     }
; }
; __device__ __forceinline__ PoolRanges pool_ranges(const Params& p, int L) {
;     const int T = moe_tiles((const int*)(p.ws + ws::CTL) + ws::CW_CNT + L * 32);
;     PoolRanges r; r.rem_up = (8 * T) & 255; r.ns_up = r.rem_up ? 256 - r.rem_up : 0; r.rem_dn = T & 63; r.ns_dn = r.rem_dn ? (64 - r.rem_dn) * 4 : 0;
;     r.beg_up = L == 0 ? POOL1_BEG : (L == 1 ? POOL2_BEG : POOL3_BEG); r.pool_end = L == 0 ? 49152 : (L == 1 ? POOL2_END : POOL3_END);
;     r.end_up = min(r.beg_up + r.ns_up * 8 * SIDE_JU, r.pool_end); r.end_dn = min(r.end_up + r.ns_dn * 8 * SIDE_JU, r.pool_end);
;     return r;
; }
; __device__ __forceinline__ void moe_up_tail(const Params& p, int L, int bid) {
;     const PoolRanges r = pool_ranges(p, L);
;     if (r.ns_up && bid >= r.rem_up) side_range(p, L + 1, r.beg_up, r.end_up, (bid - r.rem_up) * 8 + (otid() >> 6), r.ns_up * 8);
; }
; __device__ __forceinline__ void moe_down_tail(const Params& p, int L, int bid) {
;     const PoolRanges r = pool_ranges(p, L); const int j = bid >> 3, tl = (bid & 7) * 8 + (j >> 2);
;     if (r.ns_dn && tl >= r.rem_dn) side_range(p, L + 1, r.end_up, r.end_dn, ((tl - r.rem_dn) * 4 + (j & 3)) * 8 + (otid() >> 6), r.ns_dn * 8);
; }
.LBB0_1824:
	v_readlane_b32 s0, v255, 8
	v_readlane_b32 s1, v255, 9
	s_cmp_eq_u32 s0, 3
	v_readlane_b32 s4, v254, 58
	s_cselect_b64 s[0:1], -1, 0
	v_readlane_b32 s5, v254, 59
	s_or_b64 s[0:1], s[4:5], s[0:1]
	s_and_b64 vcc, exec, s[0:1]
	s_cbranch_vccnz .LBB0_1851
	s_lshl_b64 s[0:1], s[30:31], 2
	v_readlane_b32 s4, v249, 56
	v_readlane_b32 s5, v249, 57
	s_add_u32 s0, s4, s0
	s_addc_u32 s1, s5, s1
	global_load_dwordx4 v[4:7], v3, s[0:1] offset:48
	global_load_dwordx4 v[8:11], v3, s[0:1] offset:32
	global_load_dwordx4 v[12:15], v3, s[0:1] offset:16
	global_load_dwordx4 v[16:19], v3, s[0:1]
	global_load_dwordx4 v[20:23], v3, s[0:1] offset:112
	global_load_dwordx4 v[24:27], v3, s[0:1] offset:96
	global_load_dwordx4 v[28:31], v3, s[0:1] offset:80
	global_load_dwordx4 v[32:35], v3, s[0:1] offset:64
	s_waitcnt vmcnt(0)
	v_readfirstlane_b32 s4, v7
	v_readfirstlane_b32 s5, v6
	v_readfirstlane_b32 s6, v5
	v_readfirstlane_b32 s7, v4
	s_addk_i32 s7, 0xff
	s_ashr_i32 s7, s7, 8
	s_addk_i32 s6, 0xff
	s_ashr_i32 s6, s6, 8
	s_addk_i32 s5, 0xff
	s_ashr_i32 s5, s5, 8
	s_addk_i32 s4, 0xff
	s_ashr_i32 s4, s4, 8
	v_readfirstlane_b32 s8, v11
	v_readfirstlane_b32 s12, v10
	v_readfirstlane_b32 s13, v9
	v_readfirstlane_b32 s14, v8
	s_addk_i32 s14, 0xff
	s_ashr_i32 s14, s14, 8
	s_addk_i32 s13, 0xff
	s_ashr_i32 s13, s13, 8
	s_addk_i32 s12, 0xff
	s_ashr_i32 s12, s12, 8
	s_addk_i32 s8, 0xff
	s_ashr_i32 s8, s8, 8
	v_readfirstlane_b32 s15, v15
	v_readfirstlane_b32 s16, v14
	v_readfirstlane_b32 s17, v13
	v_readfirstlane_b32 s20, v12
	s_addk_i32 s20, 0xff
	s_ashr_i32 s20, s20, 8
	s_addk_i32 s17, 0xff
	s_ashr_i32 s17, s17, 8
	s_addk_i32 s16, 0xff
	s_ashr_i32 s16, s16, 8
	s_addk_i32 s15, 0xff
	s_ashr_i32 s15, s15, 8
	v_readfirstlane_b32 s21, v19
	v_readfirstlane_b32 s22, v18
	v_readfirstlane_b32 s23, v17
	v_readfirstlane_b32 s24, v16
	s_addk_i32 s24, 0xff
	s_addk_i32 s23, 0xff
	s_ashr_i32 s24, s24, 8
	s_ashr_i32 s23, s23, 8
	s_addk_i32 s22, 0xff
	s_add_i32 s23, s23, s24
	s_ashr_i32 s22, s22, 8
	s_addk_i32 s21, 0xff
	s_add_i32 s22, s23, s22
	s_ashr_i32 s21, s21, 8
	s_add_i32 s21, s22, s21
	s_add_i32 s20, s21, s20
	s_add_i32 s17, s20, s17
	s_add_i32 s16, s17, s16
	s_add_i32 s15, s16, s15
	s_add_i32 s14, s15, s14
	s_add_i32 s13, s14, s13
	s_add_i32 s12, s13, s12
	s_add_i32 s8, s12, s8
	s_add_i32 s7, s8, s7
	s_add_i32 s6, s7, s6
	s_add_i32 s8, s6, s5
	s_add_i32 s8, s8, s4
	v_readfirstlane_b32 s4, v23
	v_readfirstlane_b32 s5, v22
	v_readfirstlane_b32 s6, v21
	v_readfirstlane_b32 s7, v20
	s_addk_i32 s7, 0xff
	s_addk_i32 s6, 0xff
	s_addk_i32 s5, 0xff
	s_addk_i32 s4, 0xff
	v_readfirstlane_b32 s12, v27
	v_readfirstlane_b32 s13, v26
	v_readfirstlane_b32 s14, v25
	v_readfirstlane_b32 s15, v24
	s_addk_i32 s15, 0xff
	s_addk_i32 s14, 0xff
	s_addk_i32 s13, 0xff
	s_addk_i32 s12, 0xff
	v_readfirstlane_b32 s16, v31
	v_readfirstlane_b32 s17, v30
	v_readfirstlane_b32 s22, v29
	v_readfirstlane_b32 s23, v28
	s_addk_i32 s23, 0xff
	s_addk_i32 s22, 0xff
	s_addk_i32 s17, 0xff
	s_addk_i32 s16, 0xff
	v_readfirstlane_b32 s21, v32
	v_readfirstlane_b32 s20, v33
	s_addk_i32 s21, 0xff
	v_readfirstlane_b32 s1, v34
	s_ashr_i32 s21, s21, 8
	s_addk_i32 s20, 0xff
	v_readfirstlane_b32 s0, v35
	s_add_i32 s8, s8, s21
	s_ashr_i32 s20, s20, 8
	s_addk_i32 s1, 0xff
	s_add_i32 s8, s8, s20
	s_ashr_i32 s1, s1, 8
	s_addk_i32 s0, 0xff
	s_add_i32 s1, s8, s1
	s_ashr_i32 s0, s0, 8
	s_add_i32 s0, s1, s0
	s_ashr_i32 s8, s23, 8
	s_ashr_i32 s1, s22, 8
	s_add_i32 s0, s0, s8
	s_add_i32 s0, s0, s1
	s_ashr_i32 s8, s17, 8
	s_ashr_i32 s1, s16, 8
	s_add_i32 s0, s0, s8
	s_add_i32 s0, s0, s1
	s_ashr_i32 s8, s15, 8
	s_ashr_i32 s1, s14, 8
	s_add_i32 s0, s0, s8
	s_add_i32 s0, s0, s1
	s_ashr_i32 s8, s13, 8
	s_ashr_i32 s1, s12, 8
	s_add_i32 s0, s0, s8
	s_add_i32 s0, s0, s1
	s_ashr_i32 s1, s6, 8
	s_ashr_i32 s6, s7, 8
	s_add_i32 s0, s0, s6
	s_add_i32 s0, s0, s1
	s_ashr_i32 s1, s4, 8
	s_ashr_i32 s4, s5, 8
	s_add_i32 s5, s0, s4
	s_add_i32 s5, s5, s1
	s_and_b32 s4, s5, 63
	s_cmp_eq_u32 s4, 0
	v_readlane_b32 s6, v251, 10
	s_cselect_b64 s[0:1], -1, 0
	s_cmp_lt_i32 s6, s4
	s_cselect_b64 s[6:7], -1, 0
	s_or_b64 s[6:7], s[0:1], s[6:7]
	s_and_b64 vcc, exec, s[6:7]
	s_cbranch_vccnz .LBB0_1850
	s_lshl_b32 s6, s4, 2
	s_sub_i32 s14, 0x100, s6
	v_readlane_b32 s6, v255, 8
	v_readlane_b32 s7, v255, 9
	s_mov_b32 s8, s6
	s_cmp_eq_u32 s6, 1
	s_movk_i32 s6, 0x5c00
	s_mov_b32 s7, 0xa000
	s_cselect_b32 s6, s6, 0x9000
	s_cselect_b32 s7, s7, 0xb000
	s_cmp_eq_u32 s8, 0
	s_cselect_b32 s6, 0x1400, s6
	s_cselect_b32 s7, 0xc000, s7
	s_lshl_b32 s5, s5, 3
	s_and_b32 s5, s5, 0xf8
	s_sub_i32 s8, 0x100, s5
	s_mulk_i32 s8, 0x60
	s_cmp_lg_u32 s5, 0
	s_cselect_b32 s5, s8, 0
	s_add_i32 s5, s5, s6
	s_min_u32 s5, s5, s7
	s_mul_i32 s6, s14, 0x60
	s_and_b64 s[0:1], s[0:1], exec
	s_cselect_b32 s0, 0, s6
	s_add_i32 s0, s5, s0
	s_min_u32 s8, s0, s7
	v_readlane_b32 s0, v251, 10
	s_sub_i32 s0, s0, s4
	s_lshl_b32 s1, s0, 5
	v_readlane_b32 s21, v251, 12
	s_or_b32 s6, s1, s21
	v_mov_b32_e32 v1, v0
	s_add_i32 s6, s6, s5
	v_ashrrev_i32_e32 v2, 6, v1
	v_add_u32_e32 v1, s6, v2
	v_mov_b32_e32 v4, v0
	v_cmp_gt_i32_e32 vcc, s8, v1
	s_and_saveexec_b64 s[6:7], vcc
	s_cbranch_execz .LBB0_1849
	v_and_b32_e32 v5, 7, v4
	v_and_b32_e32 v68, 56, v4
	v_lshlrev_b32_e32 v4, 2, v5
	v_lshlrev_b32_e32 v6, 12, v5
	v_add_u32_e32 v5, s5, v2
	s_lshl_b32 s12, s14, 3
	s_lshl_b32 s16, s14, 4
	v_add_u32_e32 v69, s1, v5
	s_lshl_b32 s1, s4, 20
	v_readlane_b32 s14, v251, 55
	s_sub_i32 s1, s14, s1
	v_readlane_b32 s15, v251, 47
	s_lshl_b32 s14, s5, 15
	s_add_i32 s22, s15, s1
	s_lshl_b32 s1, s0, 6
	s_lshl_b32 s15, s5, 1
	s_lshl_b32 s0, s0, 10
	s_lshl_b32 s5, s5, 5
	s_lshl_b32 s20, s4, 14
	v_lshl_add_u32 v80, v2, 15, s14
	v_lshlrev_b32_e32 v7, 1, v2
	s_add_i32 s1, s15, s1
	v_lshlrev_b32_e32 v2, 5, v2
	s_add_i32 s0, s5, s0
	s_sub_i32 s25, 0x100000, s20
	v_readlane_b32 s20, v251, 48
	s_lshl_b32 s14, s4, 21
	v_add_u32_e32 v81, s1, v7
	s_lshl_b32 s1, s4, 7
	v_add_u32_e32 v82, s0, v2
	s_lshl_b32 s0, s4, 11
	v_add_u32_e32 v5, s20, v5
	s_lshl_b32 s20, s4, 5
	s_lshl_b32 s4, s4, 6
	v_subrev_u32_e32 v85, s4, v5
	v_readlane_b32 s4, v251, 56
	v_subrev_u32_e32 v84, s20, v5
	s_sub_i32 s23, 0x2000, s1
	v_add_u32_e32 v5, s4, v80
	v_readlane_b32 s4, v251, 51
	s_add_i32 s15, s15, s4
	v_subrev_u32_e32 v86, s14, v5
	v_add_u32_e32 v5, s15, v7
	v_subrev_u32_e32 v87, s1, v5
	v_readlane_b32 s1, v251, 52
	s_add_i32 s5, s5, s1
	v_add_u32_e32 v2, s5, v2
	s_add_i32 s13, s30, 32
	s_sub_i32 s17, 0x8000000, s14
	s_sub_i32 s24, 0x20000, s0
	v_lshlrev_b32_e32 v83, 8, v1
	v_subrev_u32_e32 v88, s0, v2
	s_mov_b64 s[14:15], 0
	v_lshlrev_b32_e32 v70, 2, v4
	v_lshlrev_b32_e32 v72, 1, v68
	v_lshlrev_b32_e32 v74, 1, v6
	s_branch .LBB0_1830
